# v35 + M0-sharing piece pairs on the B side of G1/G3/G5: each wave loads the two LDS-adjacent 1 KB sub-tiles of a half-stage with one M0 and offset:1024 on the second piece (half the B-side M0 rewrites
# speedup vs baseline: 1.0030x; 1.0030x over previous
;     __host__ __device__ bool next(int i, Unit& u) const { if (!so.next(i / 3, u)) return false; u.pn += 4 * (i % 3); u.idx = i; return true; }
; #define PG8_BAR __builtin_amdgcn_s_barrier()
; template <class Epi, class Sched, bool ALIGN_EPI = false, bool SP2 = false, bool I8 = false, bool ATILED = false>
; __device__ __forceinline__ void gemm_phase(PG8_LAS unsigned char* lds, const Gemm g, const Sched& S, const Epi& E, const int wid) {
;     ...
;     for (int i = 0; i < 2; ++i) { int R, C; stage_rc(tid * 16 + i * 8192, R, C); const int Rb = Epi::PERM ? ((R & ~31) + perm32(R & 31)) : R;
;         voffA[i] = (unsigned)(R * (ATILED ? BK : K) + C) * 2u; voffB[i] = (unsigned)(Rb * K + C) * 2u; }
;     const unsigned kstep = (unsigned)(BK * 2);
;     const unsigned hstep = (unsigned)HALF * K * 2;
;     const unsigned tstep = 2 * hstep;
;     const unsigned kstepA = ATILED ? (unsigned)(BM * BK * 2) : kstep, hstepA = ATILED ? (unsigned)(HALF * BK * 2) : hstep, tstepA = ATILED ? (unsigned)nt * (unsigned)(BM * BK * 2) : tstep;
;     const __amdgpu_buffer_rsrc_t rsA = __builtin_amdgcn_make_buffer_rsrc((void*)g.A, 0, 0x7fffffff, 0x00020000), rsB = __builtin_amdgcn_make_buffer_rsrc((void*)g.Bt, 0, 0x7fffffff, 0x00020000);
;     const unsigned ldsw = (unsigned)wid * 1024u;
;     const int aoff = lds_byte(wr * 64 + fr, fq * 8), boff = lds_byte(wc * 32 + fr, fq * 8);
;     ...
;     Unit cur, nxt; int ui = 0;
;     if (!S.next(0, cur)) return;
;     f32x4 acc[2][2][4][2];
; #pragma unroll
;     for (int a = 0; a < 2; ++a)
; #pragma unroll
;         for (int b = 0; b < 2; ++b)
; #pragma unroll
;             for (int m = 0; m < 4; ++m)
; #pragma unroll
;                 for (int n = 0; n < 2; ++n) acc[a][b][m][n] = (f32x4){0.f, 0.f, 0.f, 0.f};
;     f16x8 At[4][2], B0[2][2], B1[2][2];
;     unsigned cA = (unsigned)cur.pm * tstepA + (unsigned)(cur.pm >> 4) * g.gapA, cB = (unsigned)cur.pn * tstep;
;     S.a_ready(cur);
;     if constexpr (SP2) {
;         PG8_STAGE(PG8_SB(0, 0), rsB, cB, voffB); PG8_STAGE(PG8_SB(0, 1), rsB, cB + hstep, voffB); PG8_STAGE(PG8_SA(0, 0), rsA, cA, voffA); PG8_STAGE(PG8_SA(0, 1), rsA, cA + hstepA, voffA);
;         if (wr == 1) PG8_BAR;
;         PG8_WAIT_V(2); PG8_BAR;
;         PG8_STAGE(PG8_SB(1, 0), rsB, cB + kstep, voffB); PG8_STAGE(PG8_SA(1, 0), rsA, cA + kstepA, voffA); PG8_STAGE(PG8_SB(1, 1), rsB, cB + hstep + kstep, voffB);
;         PG8_WAIT_V(6); PG8_BAR;
.LBB0_474:
	v_readlane_b32 s28, v253, 63
	v_readlane_b32 s29, v254, 0
	s_andn2_b64 vcc, exec, s[28:29]
	v_readlane_b32 s28, v254, 1
	v_readlane_b32 s29, v254, 2
	s_waitcnt lgkmcnt(0)
	s_barrier
	v_cndmask_b32_e64 v0, 0, 1, s[28:29]
	v_cmp_ne_u32_e64 s[22:23], 1, v0
	v_mbcnt_lo_u32_b32 v2, -1, 0
	v_mbcnt_hi_u32_b32 v2, -1, v2
	s_nop 1
	v_writelane_b32 v253, s22, 31
	s_nop 1
	v_writelane_b32 v253, s23, 32
	s_cbranch_vccnz .LBB0_490
	v_lshl_add_u32 v3, v2, 4, s85
	v_ashrrev_i32_e32 v0, 31, v3
	v_lshrrev_b32_e32 v0, 22, v0
	v_add_u32_e32 v0, v3, v0
	v_ashrrev_i32_e32 v0, 10, v0
	s_waitcnt vmcnt(0)
	v_mul_i32_i24_e32 v4, 0x400, v0
	v_sub_u32_e32 v4, v3, v4
	v_lshrrev_b32_e32 v5, 4, v4
	v_bitop3_b32 v4, v5, v4, 32 bitop3:0x6c
	v_ashrrev_i32_e32 v6, 31, v4
	s_mul_hi_i32 s27, s26, 0x340000
	s_mul_i32 s26, s26, 0x340000
	v_lshrrev_b32_e32 v6, 26, v6
	s_add_u32 s26, s42, s26
	v_lshlrev_b32_e32 v5, 3, v0
	v_add_u32_e32 v6, v4, v6
	s_addc_u32 s27, s43, s27
	v_and_b32_e32 v5, -16, v5
	v_ashrrev_i32_e32 v7, 6, v6
	v_and_b32_e32 v6, 0xc0, v6
	s_add_u32 s64, s26, 0x1f000000
	v_add_u32_e32 v5, v7, v5
	v_sub_u32_e32 v4, v4, v6
	s_addc_u32 s26, s27, 0
	v_lshlrev_b32_e32 v0, 5, v0
	v_ashrrev_i16_sdwa v4, v232, sext(v4) dst_sel:DWORD dst_unused:UNUSED_PAD src0_sel:DWORD src1_sel:BYTE_0
	v_lshlrev_b32_e32 v6, 1, v5
	v_lshrrev_b32_e32 v8, 2, v5
	v_and_b32_e32 v7, 3, v7
	s_mov_b32 s27, 0x3fffe0
	v_and_b32_e32 v0, 32, v0
	v_bfe_i32 v4, v4, 0, 16
	v_and_b32_e32 v6, 24, v6
	v_and_b32_e32 v8, 4, v8
	v_and_or_b32 v7, v5, s27, v7
	v_or3_b32 v6, v7, v8, v6
	v_add_lshl_u32 v4, v0, v4, 1
	v_add_u32_e32 v3, 0x2000, v3
	v_lshl_add_u32 v0, v5, 10, v4
	v_mbcnt_lo_u32_b32 v172, -1, 0
	v_mbcnt_hi_u32_b32 v172, -1, v172
	s_lshl_b32 s100, s85, 1
	v_lshl_add_u32 v172, v172, 4, s100
	v_ashrrev_i32_e32 v4, 31, v3
	v_lshrrev_b32_e32 v4, 22, v4
	v_add_u32_e32 v4, v3, v4
	v_ashrrev_i32_e32 v4, 10, v4
	v_mul_i32_i24_e32 v5, 0x400, v4
	v_sub_u32_e32 v3, v3, v5
	v_lshrrev_b32_e32 v5, 4, v3
	v_bitop3_b32 v3, v5, v3, 32 bitop3:0x6c
	v_ashrrev_i32_e32 v6, 31, v3
	v_lshrrev_b32_e32 v6, 26, v6
	v_add_u32_e32 v6, v3, v6
	v_ashrrev_i32_e32 v7, 6, v6
	v_and_b32_e32 v6, 0xffc0, v6
	v_sub_u32_e32 v3, v3, v6
	v_lshlrev_b32_e32 v5, 3, v4
	v_lshrrev_b16_e32 v6, 7, v3
	v_and_b32_e32 v5, -16, v5
	v_and_b32_e32 v6, 1, v6
	v_add_u32_e32 v5, v7, v5
	v_add_u16_e32 v3, v3, v6
	s_and_b32 s65, s26, 0xffff
	s_mov_b32 s26, s85
	v_lshlrev_b32_e32 v4, 5, v4
	v_ashrrev_i16_sdwa v3, v232, sext(v3) dst_sel:DWORD dst_unused:UNUSED_PAD src0_sel:DWORD src1_sel:BYTE_0
	v_lshlrev_b32_e32 v6, 1, v5
	v_lshrrev_b32_e32 v8, 2, v5
	v_and_b32_e32 v7, 3, v7
	v_and_b32_e32 v4, 32, v4
	v_bfe_i32 v3, v3, 0, 16
	v_and_b32_e32 v6, 24, v6
	v_and_b32_e32 v8, 4, v8
	v_and_or_b32 v7, v5, s27, v7
	s_lshl1_add_u32 m0, s85, 0x10000
	v_readlane_b32 s27, v254, 29
	s_bfe_u32 s100, s27, 0x10011
	s_bfe_u32 s101, s27, 0x10007
	s_and_b32 s27, s27, 0xfffc0000
	s_lshl_b32 s100, s100, 14
	s_lshl_b32 s101, s101, 15
	s_or_b32 s27, s27, s100
	s_or_b32 s27, s27, s101
	s_mov_b32 s26, s85
	v_or3_b32 v6, v7, v8, v6
	v_add_lshl_u32 v3, v4, v3, 1
	v_mbcnt_lo_u32_b32 v174, -1, 0
	v_mbcnt_hi_u32_b32 v174, -1, v174
	v_lshl_add_u32 v174, v174, 4, s85
	v_add_u32_e32 v174, 0x2000, v174
	s_mov_b32 s90, s66
	buffer_load_dwordx4 v172, s[64:67], s27 offen lds
	s_mov_b32 s26, s85
	buffer_load_dwordx4 v172, s[64:67], s27 offen offset:1024 lds
	s_lshl1_add_u32 m0, s85, 0x14000
	v_readlane_b32 s27, v254, 23
	s_bfe_u32 s100, s27, 0x10011
	s_bfe_u32 s101, s27, 0x10007
	s_and_b32 s27, s27, 0xfffc0000
	s_lshl_b32 s100, s100, 14
	s_lshl_b32 s101, s101, 15
	s_or_b32 s27, s27, s100
	s_or_b32 s27, s27, s101
	s_mov_b32 s26, s85
	s_mov_b32 s91, s67
	v_lshl_add_u32 v173, v5, 10, v3
	v_readlane_b32 s22, v253, 31
	v_readlane_b32 s23, v253, 32
	buffer_load_dwordx4 v172, s[64:67], s27 offen lds
	s_mov_b32 s26, s85
	buffer_load_dwordx4 v172, s[64:67], s27 offen offset:1024 lds
	s_mov_b32 m0, s26
	v_readlane_b32 s27, v254, 27
	s_mov_b32 s26, s85
	s_and_b64 vcc, exec, s[22:23]
	s_nop 2
	buffer_load_dwordx4 v0, s[88:91], s27 offen lds
	s_add_i32 m0, s26, 0x2000
	s_mov_b32 s26, s85
	buffer_load_dwordx4 v173, s[88:91], s27 offen lds
	s_add_i32 m0, s26, 0x4000
	v_readlane_b32 s27, v254, 25
	s_mov_b32 s26, s85
	s_nop 3
	buffer_load_dwordx4 v0, s[88:91], s27 offen lds
	s_add_i32 m0, s26, 0x6000
	s_nop 0
	buffer_load_dwordx4 v173, s[88:91], s27 offen lds
	s_cbranch_vccnz .LBB0_477
	s_barrier
.LBB0_477:
	s_mov_b32 s26, s85
	s_add_u32 s34, s40, 0xe800000
	s_waitcnt vmcnt(2)
	s_barrier
	s_addc_u32 s35, s41, 0
	s_lshl1_add_u32 m0, s85, 0x18000
	v_readlane_b32 s27, v254, 26
	s_bfe_u32 s100, s27, 0x10011
	s_bfe_u32 s101, s27, 0x10007
	s_and_b32 s27, s27, 0xfffc0000
	s_lshl_b32 s100, s100, 14
	s_lshl_b32 s101, s101, 15
	s_or_b32 s27, s27, s100
	s_or_b32 s27, s27, s101
	s_mov_b32 s26, s85
	v_and_b32_e32 v175, 15, v2
	v_or_b32_e32 v176, s96, v175
	v_lshlrev_b32_e32 v5, 6, v176
	v_and_b32_e32 v6, 48, v2
	buffer_load_dwordx4 v172, s[64:67], s27 offen lds
	s_mov_b32 s26, s85
	buffer_load_dwordx4 v172, s[64:67], s27 offen offset:1024 lds
	s_add_i32 m0, s26, 0x8000
	v_readlane_b32 s27, v254, 28
	s_mov_b32 s26, s85
	v_ashrrev_i32_e32 v4, 6, v2
	v_ashrrev_i32_e32 v3, 1, v2
	v_lshlrev_b32_e32 v8, 2, v176
	v_and_b32_e32 v3, -8, v3
	buffer_load_dwordx4 v0, s[88:91], s27 offen lds
	s_add_i32 m0, s26, 0xa000
	s_mov_b32 s26, s85
	buffer_load_dwordx4 v173, s[88:91], s27 offen lds
	s_lshl1_add_u32 m0, s85, 0x1c000
	v_readlane_b32 s27, v254, 30
	s_bfe_u32 s100, s27, 0x10011
	s_bfe_u32 s101, s27, 0x10007
	s_and_b32 s27, s27, 0xfffc0000
	s_lshl_b32 s100, s100, 14
	s_lshl_b32 s101, s101, 15
	s_or_b32 s27, s27, s100
	s_or_b32 s27, s27, s101
	s_mov_b32 s26, s85
	v_and_b32_e32 v8, 32, v8
	v_lshlrev_b32_e32 v2, 2, v2
	v_and_b32_e32 v2, 32, v2
	s_mov_b32 s44, 0
	buffer_load_dwordx4 v172, s[64:67], s27 offen lds
	s_movk_i32 s26, 0x3c0
	buffer_load_dwordx4 v172, s[64:67], s27 offen offset:1024 lds
	v_and_or_b32 v5, v5, s26, v6
	v_readlane_b32 s26, v253, 60
	s_waitcnt vmcnt(6)
	v_readlane_b32 s42, v254, 22
	v_readlane_b32 s43, v254, 24
	v_lshl_add_u32 v7, v4, 10, s26
	v_readlane_b32 s26, v253, 62
	v_bitop3_b32 v177, v5, v7, v8 bitop3:0xde
	v_lshl_or_b32 v5, v175, 6, v6
	v_add_lshl_u32 v4, v4, s26, 10
	v_readlane_b32 s26, v253, 61
	v_bitop3_b32 v178, v5, v4, v2 bitop3:0xde
	v_readlane_b32 s48, v254, 29
	v_add_u32_e32 v179, s26, v3
	v_lshlrev_b32_e32 v2, 2, v179
	v_add_u32_e32 v180, 0x22400, v2
	v_add_u32_e32 v181, 0x24400, v2
	v_readlane_b32 s47, v254, 27
	s_mov_b32 s49, 0
	s_barrier
	s_branch .LBB0_480

; #define PG8_STAGE(bufoff, RS, soff, voff) do { _Pragma("unroll") for (int _i = 0; _i < 2; ++_i) \
;         __builtin_amdgcn_raw_ptr_buffer_load_lds(RS, (PG8_LAS void*)(lds + (bufoff) + sgpr_opaque(ldsw) + _i * 8192), 16, (int)(voff)[_i], (int)(soff), 0, 0); } while (0)
; #define PG8_LDA(dst, b, h) do { _Pragma("unroll") for (int m = 0; m < 4; ++m) _Pragma("unroll") for (int k = 0; k < 2; ++k) dst[m][k] = *(const PG8_LAS f16x8*)(lds + PG8_SA(b, h) + aoff + m * 2048 + k * 1024); } while (0)
; #define PG8_WAIT_L(n) asm volatile("s_waitcnt lgkmcnt(" #n ")" ::: "memory")
; #define PG8_BAR __builtin_amdgcn_s_barrier()
; #define PG8_SCHED __builtin_amdgcn_sched_barrier(0)
; template <class Epi, class Sched, bool ALIGN_EPI = false, bool SP2 = false, bool I8 = false, bool ATILED = false>
; __device__ __forceinline__ void gemm_phase(PG8_LAS unsigned char* lds, const Gemm g, const Sched& S, const Epi& E, const int wid) {
;     ...
;             PG8_WAIT_VG; PG8_WAIT_L(0); PG8_BAR; PG8_MMA(0, 0, At, B0); PG8_MMA(0, 1, At, B1); PG8_BAR; PG8_SCHED;
;             PG8_LDA(At, 0, 1); PG8_STAGE(PG8_SB(0, 0), rsB, b2, voffB); PG8_STAGE(PG8_SB(0, 1), rsB, b2 + hstep, voffB); PG8_STAGE(PG8_SA(0, 0), rsA, a2, voffA);
.Lgr0:
	s_waitcnt vmcnt(24)
	s_waitcnt lgkmcnt(0)
	s_barrier
	s_setprio 1
	s_waitcnt lgkmcnt(7)
	v_mfma_i32_16x16x64_i8 v[126:129], v[130:133], v[162:165], v[126:129]
	v_mfma_i32_16x16x64_i8 v[122:125], v[138:141], v[162:165], v[122:125]
	s_waitcnt lgkmcnt(5)
	v_mfma_i32_16x16x64_i8 v[110:113], v[130:133], v[182:185], v[110:113]
	v_mfma_i32_16x16x64_i8 v[106:109], v[138:141], v[182:185], v[106:109]
	s_waitcnt lgkmcnt(3)
	v_mfma_i32_16x16x64_i8 v[94:97], v[130:133], v[190:193], v[94:97]
	v_mfma_i32_16x16x64_i8 v[90:93], v[138:141], v[190:193], v[90:93]
	s_waitcnt lgkmcnt(1)
	v_mfma_i32_16x16x64_i8 v[78:81], v[130:133], v[208:211], v[78:81]
	v_mfma_i32_16x16x64_i8 v[74:77], v[138:141], v[208:211], v[74:77]
	v_mfma_i32_16x16x64_i8 v[126:129], v[134:137], v[166:169], v[126:129]
	v_mfma_i32_16x16x64_i8 v[122:125], v[142:145], v[166:169], v[122:125]
	v_mfma_i32_16x16x64_i8 v[110:113], v[134:137], v[186:189], v[110:113]
	v_mfma_i32_16x16x64_i8 v[106:109], v[142:145], v[186:189], v[106:109]
	v_mfma_i32_16x16x64_i8 v[94:97], v[134:137], v[194:197], v[94:97]
	v_mfma_i32_16x16x64_i8 v[90:93], v[142:145], v[194:197], v[90:93]
	s_waitcnt lgkmcnt(0)
	v_mfma_i32_16x16x64_i8 v[78:81], v[134:137], v[212:215], v[78:81]
	v_mfma_i32_16x16x64_i8 v[74:77], v[142:145], v[212:215], v[74:77]
	s_setprio 0
	s_setprio 1
	v_mfma_i32_16x16x64_i8 v[118:121], v[146:149], v[162:165], v[118:121]
	v_mfma_i32_16x16x64_i8 v[114:117], v[154:157], v[162:165], v[114:117]
	v_mfma_i32_16x16x64_i8 v[102:105], v[146:149], v[182:185], v[102:105]
	v_mfma_i32_16x16x64_i8 v[98:101], v[154:157], v[182:185], v[98:101]
	v_mfma_i32_16x16x64_i8 v[86:89], v[146:149], v[190:193], v[86:89]
	v_mfma_i32_16x16x64_i8 v[82:85], v[154:157], v[190:193], v[82:85]
	v_mfma_i32_16x16x64_i8 v[70:73], v[146:149], v[208:211], v[70:73]
	v_mfma_i32_16x16x64_i8 v[66:69], v[154:157], v[208:211], v[66:69]
	v_mfma_i32_16x16x64_i8 v[118:121], v[150:153], v[166:169], v[118:121]
	v_mfma_i32_16x16x64_i8 v[114:117], v[158:161], v[166:169], v[114:117]
	v_mfma_i32_16x16x64_i8 v[102:105], v[150:153], v[186:189], v[102:105]
	v_mfma_i32_16x16x64_i8 v[98:101], v[158:161], v[186:189], v[98:101]
	v_mfma_i32_16x16x64_i8 v[86:89], v[150:153], v[194:197], v[86:89]
	v_mfma_i32_16x16x64_i8 v[82:85], v[158:161], v[194:197], v[82:85]
	v_mfma_i32_16x16x64_i8 v[70:73], v[150:153], v[212:215], v[70:73]
	v_mfma_i32_16x16x64_i8 v[66:69], v[158:161], v[212:215], v[66:69]
	s_setprio 0
	s_barrier
	s_mov_b32 s55, s85
	ds_read_b128 v[162:165], v177 offset:16384
	ds_read_b128 v[166:169], v177 offset:17408
	ds_read_b128 v[182:185], v177 offset:18432
	ds_read_b128 v[186:189], v177 offset:19456
	ds_read_b128 v[190:193], v177 offset:20480
	ds_read_b128 v[194:197], v177 offset:21504
	ds_read_b128 v[208:211], v177 offset:22528
	ds_read_b128 v[212:215], v177 offset:23552
	s_lshl1_add_u32 m0, s85, 0x10000
	s_mov_b32 s55, s85
	buffer_load_dwordx4 v172, s[64:67], s51 offen lds
	s_mov_b32 s58, s85
	buffer_load_dwordx4 v172, s[64:67], s51 offen offset:1024 lds
	s_add_i32 s55, s51, 0x4000
	s_lshl1_add_u32 m0, s85, 0x14000
	s_mov_b32 s58, s85
	buffer_load_dwordx4 v172, s[64:67], s55 offen lds
	s_nop 0
	buffer_load_dwordx4 v172, s[64:67], s55 offen offset:1024 lds
	s_mov_b32 s55, s85
	s_mov_b32 m0, s55
	s_mov_b32 s55, s85
	buffer_load_dwordx4 v0, s[88:91], s54 offen lds
	s_add_i32 m0, s55, 0x2000
	s_nop 0
	buffer_load_dwordx4 v173, s[88:91], s54 offen lds
	s_cmp_lg_u32 s53, 0
	s_cbranch_scc1 .Lgr1
	s_waitcnt vmcnt(8)

; #define PG8_STAGE(bufoff, RS, soff, voff) do { _Pragma("unroll") for (int _i = 0; _i < 2; ++_i) \
;         __builtin_amdgcn_raw_ptr_buffer_load_lds(RS, (PG8_LAS void*)(lds + (bufoff) + sgpr_opaque(ldsw) + _i * 8192), 16, (int)(voff)[_i], (int)(soff), 0, 0); } while (0)
; #define PG8_LDA(dst, b, h) do { _Pragma("unroll") for (int m = 0; m < 4; ++m) _Pragma("unroll") for (int k = 0; k < 2; ++k) dst[m][k] = *(const PG8_LAS f16x8*)(lds + PG8_SA(b, h) + aoff + m * 2048 + k * 1024); } while (0)
; #define PG8_WAIT_L(n) asm volatile("s_waitcnt lgkmcnt(" #n ")" ::: "memory")
; #define PG8_BAR __builtin_amdgcn_s_barrier()
; #define PG8_SCHED __builtin_amdgcn_sched_barrier(0)
; template <class Epi, class Sched, bool ALIGN_EPI = false, bool SP2 = false, bool I8 = false, bool ATILED = false>
; __device__ __forceinline__ void gemm_phase(PG8_LAS unsigned char* lds, const Gemm g, const Sched& S, const Epi& E, const int wid) {
;     ...
;             PG8_WAIT_VG; PG8_WAIT_L(0); PG8_BAR; PG8_MMA(0, 0, At, B0); PG8_MMA(0, 1, At, B1); PG8_BAR; PG8_SCHED;
;             PG8_LDA(At, 1, 1); PG8_STAGE(PG8_SB(1, 0), rsB, b3, voffB); PG8_STAGE(PG8_SB(1, 1), rsB, b3 + hstep, voffB); PG8_STAGE(PG8_SA(1, 0), rsA, a3, voffA);
.Lgr2:
	s_waitcnt vmcnt(24)
	s_waitcnt lgkmcnt(0)
	s_barrier
	s_setprio 1
	s_waitcnt lgkmcnt(7)
	v_mfma_i32_16x16x64_i8 v[126:129], v[130:133], v[162:165], v[126:129]
	v_mfma_i32_16x16x64_i8 v[122:125], v[138:141], v[162:165], v[122:125]
	s_waitcnt lgkmcnt(5)
	v_mfma_i32_16x16x64_i8 v[110:113], v[130:133], v[182:185], v[110:113]
	v_mfma_i32_16x16x64_i8 v[106:109], v[138:141], v[182:185], v[106:109]
	s_waitcnt lgkmcnt(3)
	v_mfma_i32_16x16x64_i8 v[94:97], v[130:133], v[190:193], v[94:97]
	v_mfma_i32_16x16x64_i8 v[90:93], v[138:141], v[190:193], v[90:93]
	s_waitcnt lgkmcnt(1)
	v_mfma_i32_16x16x64_i8 v[78:81], v[130:133], v[208:211], v[78:81]
	v_mfma_i32_16x16x64_i8 v[74:77], v[138:141], v[208:211], v[74:77]
	v_mfma_i32_16x16x64_i8 v[126:129], v[134:137], v[166:169], v[126:129]
	v_mfma_i32_16x16x64_i8 v[122:125], v[142:145], v[166:169], v[122:125]
	v_mfma_i32_16x16x64_i8 v[110:113], v[134:137], v[186:189], v[110:113]
	v_mfma_i32_16x16x64_i8 v[106:109], v[142:145], v[186:189], v[106:109]
	v_mfma_i32_16x16x64_i8 v[94:97], v[134:137], v[194:197], v[94:97]
	v_mfma_i32_16x16x64_i8 v[90:93], v[142:145], v[194:197], v[90:93]
	s_waitcnt lgkmcnt(0)
	v_mfma_i32_16x16x64_i8 v[78:81], v[134:137], v[212:215], v[78:81]
	v_mfma_i32_16x16x64_i8 v[74:77], v[142:145], v[212:215], v[74:77]
	s_setprio 0
	s_setprio 1
	v_mfma_i32_16x16x64_i8 v[118:121], v[146:149], v[162:165], v[118:121]
	v_mfma_i32_16x16x64_i8 v[114:117], v[154:157], v[162:165], v[114:117]
	v_mfma_i32_16x16x64_i8 v[102:105], v[146:149], v[182:185], v[102:105]
	v_mfma_i32_16x16x64_i8 v[98:101], v[154:157], v[182:185], v[98:101]
	v_mfma_i32_16x16x64_i8 v[86:89], v[146:149], v[190:193], v[86:89]
	v_mfma_i32_16x16x64_i8 v[82:85], v[154:157], v[190:193], v[82:85]
	v_mfma_i32_16x16x64_i8 v[70:73], v[146:149], v[208:211], v[70:73]
	v_mfma_i32_16x16x64_i8 v[66:69], v[154:157], v[208:211], v[66:69]
	v_mfma_i32_16x16x64_i8 v[118:121], v[150:153], v[166:169], v[118:121]
	v_mfma_i32_16x16x64_i8 v[114:117], v[158:161], v[166:169], v[114:117]
	v_mfma_i32_16x16x64_i8 v[102:105], v[150:153], v[186:189], v[102:105]
	v_mfma_i32_16x16x64_i8 v[98:101], v[158:161], v[186:189], v[98:101]
	v_mfma_i32_16x16x64_i8 v[86:89], v[150:153], v[194:197], v[86:89]
	v_mfma_i32_16x16x64_i8 v[82:85], v[158:161], v[194:197], v[82:85]
	v_mfma_i32_16x16x64_i8 v[70:73], v[150:153], v[212:215], v[70:73]
	v_mfma_i32_16x16x64_i8 v[66:69], v[158:161], v[212:215], v[66:69]
	s_setprio 0
	s_barrier
	s_mov_b32 s54, s85
	ds_read_b128 v[162:165], v177 offset:49152
	ds_read_b128 v[166:169], v177 offset:50176
	ds_read_b128 v[182:185], v177 offset:51200
	ds_read_b128 v[186:189], v177 offset:52224
	ds_read_b128 v[190:193], v177 offset:53248
	ds_read_b128 v[194:197], v177 offset:54272
	ds_read_b128 v[208:211], v177 offset:55296
	ds_read_b128 v[212:215], v177 offset:56320
	s_lshl1_add_u32 m0, s85, 0x18000
	s_mov_b32 s54, s85
	buffer_load_dwordx4 v172, s[64:67], s52 offen lds
	s_add_i32 s51, s51, 0xc000
	buffer_load_dwordx4 v172, s[64:67], s52 offen offset:1024 lds
	s_mov_b32 s52, s85
	s_lshl1_add_u32 m0, s85, 0x1c000
	s_mov_b32 s52, s85
	buffer_load_dwordx4 v172, s[64:67], s51 offen lds
	s_nop 0
	buffer_load_dwordx4 v172, s[64:67], s51 offen offset:1024 lds
	s_mov_b32 s51, s85
	s_add_i32 m0, s51, 0x8000
	s_mov_b32 s51, s85
	buffer_load_dwordx4 v0, s[88:91], s50 offen lds
	s_add_i32 m0, s51, 0xa000
	s_nop 0
	buffer_load_dwordx4 v173, s[88:91], s50 offen lds
	s_cmp_lg_u32 s53, 0
	s_cbranch_scc1 .Lgr3
	s_waitcnt vmcnt(8)

;     __host__ __device__ bool next(int i, Unit& u) const { if (!so.next(i / 3, u)) return false; u.pn += 4 * (i % 3); u.idx = i; return true; }
; #define PG8_BAR __builtin_amdgcn_s_barrier()
; template <class Epi, class Sched, bool ALIGN_EPI = false, bool SP2 = false, bool I8 = false, bool ATILED = false>
; __device__ __forceinline__ void gemm_phase(PG8_LAS unsigned char* lds, const Gemm g, const Sched& S, const Epi& E, const int wid) {
;     ...
;     for (int i = 0; i < 2; ++i) { int R, C; stage_rc(tid * 16 + i * 8192, R, C); const int Rb = Epi::PERM ? ((R & ~31) + perm32(R & 31)) : R;
;         voffA[i] = (unsigned)(R * (ATILED ? BK : K) + C) * 2u; voffB[i] = (unsigned)(Rb * K + C) * 2u; }
;     const unsigned kstep = (unsigned)(BK * 2);
;     const unsigned hstep = (unsigned)HALF * K * 2;
;     const unsigned tstep = 2 * hstep;
;     const unsigned kstepA = ATILED ? (unsigned)(BM * BK * 2) : kstep, hstepA = ATILED ? (unsigned)(HALF * BK * 2) : hstep, tstepA = ATILED ? (unsigned)nt * (unsigned)(BM * BK * 2) : tstep;
;     const __amdgpu_buffer_rsrc_t rsA = __builtin_amdgcn_make_buffer_rsrc((void*)g.A, 0, 0x7fffffff, 0x00020000), rsB = __builtin_amdgcn_make_buffer_rsrc((void*)g.Bt, 0, 0x7fffffff, 0x00020000);
;     const unsigned ldsw = (unsigned)wid * 1024u;
;     const int aoff = lds_byte(wr * 64 + fr, fq * 8), boff = lds_byte(wc * 32 + fr, fq * 8);
;     ...
;     Unit cur, nxt; int ui = 0;
;     if (!S.next(0, cur)) return;
;     f32x4 acc[2][2][4][2];
; #pragma unroll
;     for (int a = 0; a < 2; ++a)
; #pragma unroll
;         for (int b = 0; b < 2; ++b)
; #pragma unroll
;             for (int m = 0; m < 4; ++m)
; #pragma unroll
;                 for (int n = 0; n < 2; ++n) acc[a][b][m][n] = (f32x4){0.f, 0.f, 0.f, 0.f};
;     f16x8 At[4][2], B0[2][2], B1[2][2];
;     unsigned cA = (unsigned)cur.pm * tstepA + (unsigned)(cur.pm >> 4) * g.gapA, cB = (unsigned)cur.pn * tstep;
;     S.a_ready(cur);
;     if constexpr (SP2) {
;         PG8_STAGE(PG8_SB(0, 0), rsB, cB, voffB); PG8_STAGE(PG8_SB(0, 1), rsB, cB + hstep, voffB); PG8_STAGE(PG8_SA(0, 0), rsA, cA, voffA); PG8_STAGE(PG8_SA(0, 1), rsA, cA + hstepA, voffA);
;         if (wr == 1) PG8_BAR;
;         PG8_WAIT_V(2); PG8_BAR;
;         PG8_STAGE(PG8_SB(1, 0), rsB, cB + kstep, voffB); PG8_STAGE(PG8_SA(1, 0), rsA, cA + kstepA, voffA); PG8_STAGE(PG8_SB(1, 1), rsB, cB + hstep + kstep, voffB);
;         PG8_WAIT_V(6); PG8_BAR;
.LBB0_1210:
	s_and_b64 vcc, exec, s[30:31]
	s_waitcnt lgkmcnt(0)
	s_barrier
	v_mbcnt_lo_u32_b32 v2, -1, 0
	v_mbcnt_hi_u32_b32 v2, -1, v2
	s_cbranch_vccnz .LBB0_1297
	v_lshl_add_u32 v3, v2, 4, s85
	v_ashrrev_i32_e32 v0, 31, v3
	v_lshrrev_b32_e32 v0, 22, v0
	v_add_u32_e32 v0, v3, v0
	v_ashrrev_i32_e32 v0, 10, v0
	s_waitcnt vmcnt(0)
	v_mul_i32_i24_e32 v4, 0x400, v0
	v_sub_u32_e32 v4, v3, v4
	v_lshrrev_b32_e32 v5, 4, v4
	v_bitop3_b32 v4, v5, v4, 32 bitop3:0x6c
	v_ashrrev_i32_e32 v6, 31, v4
	s_mul_hi_i32 s27, s26, 0x300000
	s_mul_i32 s26, s26, 0x300000
	v_lshrrev_b32_e32 v6, 26, v6
	s_add_u32 s26, s48, s26
	v_lshlrev_b32_e32 v5, 3, v0
	v_add_u32_e32 v6, v4, v6
	s_addc_u32 s27, s49, s27
	v_and_b32_e32 v5, -16, v5
	v_ashrrev_i32_e32 v7, 6, v6
	v_and_b32_e32 v6, 0xc0, v6
	s_add_u32 s64, s26, 0x1ea00000
	v_add_u32_e32 v5, v7, v5
	v_sub_u32_e32 v4, v4, v6
	s_addc_u32 s26, s27, 0
	v_lshlrev_b32_e32 v0, 5, v0
	v_ashrrev_i16_sdwa v4, v232, sext(v4) dst_sel:DWORD dst_unused:UNUSED_PAD src0_sel:DWORD src1_sel:BYTE_0
	v_lshlrev_b32_e32 v6, 1, v5
	v_lshrrev_b32_e32 v8, 2, v5
	v_and_b32_e32 v7, 3, v7
	s_mov_b32 s27, 0x3fffe0
	v_and_b32_e32 v0, 32, v0
	v_bfe_i32 v4, v4, 0, 16
	v_and_b32_e32 v6, 24, v6
	v_and_b32_e32 v8, 4, v8
	v_and_or_b32 v7, v5, s27, v7
	v_or3_b32 v6, v7, v8, v6
	v_add_lshl_u32 v4, v0, v4, 1
	v_add_u32_e32 v3, 0x2000, v3
	v_lshl_add_u32 v0, v5, 10, v4
	v_mbcnt_lo_u32_b32 v194, -1, 0
	v_mbcnt_hi_u32_b32 v194, -1, v194
	s_lshl_b32 s100, s85, 1
	v_lshl_add_u32 v194, v194, 4, s100
	v_ashrrev_i32_e32 v4, 31, v3
	v_lshrrev_b32_e32 v4, 22, v4
	v_add_u32_e32 v4, v3, v4
	v_ashrrev_i32_e32 v4, 10, v4
	v_mul_i32_i24_e32 v5, 0x400, v4
	v_sub_u32_e32 v3, v3, v5
	v_lshrrev_b32_e32 v5, 4, v3
	v_bitop3_b32 v3, v5, v3, 32 bitop3:0x6c
	v_ashrrev_i32_e32 v6, 31, v3
	v_lshrrev_b32_e32 v6, 26, v6
	v_add_u32_e32 v6, v3, v6
	v_ashrrev_i32_e32 v7, 6, v6
	v_and_b32_e32 v6, 0xffc0, v6
	v_sub_u32_e32 v3, v3, v6
	v_lshlrev_b32_e32 v5, 3, v4
	v_lshrrev_b16_e32 v6, 7, v3
	v_and_b32_e32 v5, -16, v5
	v_and_b32_e32 v6, 1, v6
	v_add_u32_e32 v5, v7, v5
	v_add_u16_e32 v3, v3, v6
	s_and_b32 s65, s26, 0xffff
	s_mov_b32 s26, s85
	v_lshlrev_b32_e32 v4, 5, v4
	v_ashrrev_i16_sdwa v3, v232, sext(v3) dst_sel:DWORD dst_unused:UNUSED_PAD src0_sel:DWORD src1_sel:BYTE_0
	v_lshlrev_b32_e32 v6, 1, v5
	v_lshrrev_b32_e32 v8, 2, v5
	v_and_b32_e32 v7, 3, v7
	v_and_b32_e32 v4, 32, v4
	v_bfe_i32 v3, v3, 0, 16
	v_and_b32_e32 v6, 24, v6
	v_and_b32_e32 v8, 4, v8
	v_and_or_b32 v7, v5, s27, v7
	s_lshl1_add_u32 m0, s85, 0x10000
	v_readlane_b32 s27, v255, 3
	s_bfe_u32 s100, s27, 0x10011
	s_bfe_u32 s101, s27, 0x10007
	s_and_b32 s27, s27, 0xfffc0000
	s_lshl_b32 s100, s100, 14
	s_lshl_b32 s101, s101, 15
	s_or_b32 s27, s27, s100
	s_or_b32 s27, s27, s101
	s_mov_b32 s26, s85
	v_or3_b32 v6, v7, v8, v6
	v_add_lshl_u32 v3, v4, v3, 1
	v_mbcnt_lo_u32_b32 v196, -1, 0
	v_mbcnt_hi_u32_b32 v196, -1, v196
	v_lshl_add_u32 v196, v196, 4, s85
	v_add_u32_e32 v196, 0x2000, v196
	s_mov_b32 s90, s66
	buffer_load_dwordx4 v194, s[64:67], s27 offen lds
	s_mov_b32 s26, s85
	buffer_load_dwordx4 v194, s[64:67], s27 offen offset:1024 lds
	s_lshl1_add_u32 m0, s85, 0x14000
	v_readlane_b32 s27, v254, 61
	s_bfe_u32 s100, s27, 0x10011
	s_bfe_u32 s101, s27, 0x10007
	s_and_b32 s27, s27, 0xfffc0000
	s_lshl_b32 s100, s100, 14
	s_lshl_b32 s101, s101, 15
	s_or_b32 s27, s27, s100
	s_or_b32 s27, s27, s101
	s_mov_b32 s26, s85
	s_mov_b32 s91, s67
	v_lshl_add_u32 v195, v5, 10, v3
	v_readlane_b32 s22, v253, 31
	v_readlane_b32 s23, v253, 32
	buffer_load_dwordx4 v194, s[64:67], s27 offen lds
	s_mov_b32 s26, s85
	buffer_load_dwordx4 v194, s[64:67], s27 offen offset:1024 lds
	s_mov_b32 m0, s26
	v_readlane_b32 s27, v255, 1
	s_mov_b32 s26, s85
	s_and_b64 vcc, exec, s[22:23]
	s_nop 2
	buffer_load_dwordx4 v0, s[88:91], s27 offen lds
	s_add_i32 m0, s26, 0x2000
	s_mov_b32 s26, s85
	buffer_load_dwordx4 v195, s[88:91], s27 offen lds
	s_add_i32 m0, s26, 0x4000
	v_readlane_b32 s27, v254, 63
	s_mov_b32 s26, s85
	s_nop 3
	buffer_load_dwordx4 v0, s[88:91], s27 offen lds
	s_add_i32 m0, s26, 0x6000
	s_nop 0
	buffer_load_dwordx4 v195, s[88:91], s27 offen lds
	s_cbranch_vccnz .LBB0_1213
	s_barrier
.LBB0_1213:
	s_add_u32 s40, s44, 0xe800000
	s_addc_u32 s41, s45, 0
	s_mov_b32 s26, s85
	s_add_u32 s42, s46, 0x10000000
	s_waitcnt vmcnt(2)
	s_barrier
	s_addc_u32 s43, s47, 0
	s_lshl1_add_u32 m0, s85, 0x18000
	v_readlane_b32 s27, v255, 0
	s_bfe_u32 s100, s27, 0x10011
	s_bfe_u32 s101, s27, 0x10007
	s_and_b32 s27, s27, 0xfffc0000
	s_lshl_b32 s100, s100, 14
	s_lshl_b32 s101, s101, 15
	s_or_b32 s27, s27, s100
	s_or_b32 s27, s27, s101
	s_mov_b32 s26, s85
	v_and_b32_e32 v197, 15, v2
	v_or_b32_e32 v208, s96, v197
	v_lshlrev_b32_e32 v5, 6, v208
	v_and_b32_e32 v6, 48, v2
	buffer_load_dwordx4 v194, s[64:67], s27 offen lds
	s_mov_b32 s26, s85
	buffer_load_dwordx4 v194, s[64:67], s27 offen offset:1024 lds
	s_add_i32 m0, s26, 0x8000
	v_readlane_b32 s27, v255, 2
	s_mov_b32 s26, s85
	v_ashrrev_i32_e32 v4, 6, v2
	v_ashrrev_i32_e32 v3, 1, v2
	v_lshlrev_b32_e32 v8, 2, v208
	v_and_b32_e32 v3, -8, v3
	buffer_load_dwordx4 v0, s[88:91], s27 offen lds
	s_add_i32 m0, s26, 0xa000
	s_mov_b32 s26, s85
	buffer_load_dwordx4 v195, s[88:91], s27 offen lds
	s_lshl1_add_u32 m0, s85, 0x1c000
	v_readlane_b32 s27, v255, 4
	s_bfe_u32 s100, s27, 0x10011
	s_bfe_u32 s101, s27, 0x10007
	s_and_b32 s27, s27, 0xfffc0000
	s_lshl_b32 s100, s100, 14
	s_lshl_b32 s101, s101, 15
	s_or_b32 s27, s27, s100
	s_or_b32 s27, s27, s101
	s_mov_b32 s26, s85
	v_and_b32_e32 v8, 32, v8
	v_lshlrev_b32_e32 v2, 2, v2
	v_and_b32_e32 v2, 32, v2
	s_mov_b32 s46, 0
	buffer_load_dwordx4 v194, s[64:67], s27 offen lds
	s_movk_i32 s26, 0x3c0
	buffer_load_dwordx4 v194, s[64:67], s27 offen offset:1024 lds
	v_and_or_b32 v5, v5, s26, v6
	v_readlane_b32 s26, v253, 60
	s_waitcnt vmcnt(6)
	s_add_u32 s44, s44, 0xf000000
	s_addc_u32 s45, s45, 0
	v_lshl_add_u32 v7, v4, 10, s26
	v_readlane_b32 s26, v253, 62
	v_bitop3_b32 v209, v5, v7, v8 bitop3:0xde
	v_lshl_or_b32 v5, v197, 6, v6
	v_add_lshl_u32 v4, v4, s26, 10
	v_readlane_b32 s26, v253, 61
	v_bitop3_b32 v210, v5, v4, v2 bitop3:0xde
	v_readlane_b32 s47, v254, 60
	v_add_u32_e32 v237, s26, v3
	v_lshlrev_b32_e32 v2, 2, v237
	v_add_u32_e32 v199, 0x22400, v2
	v_add_u32_e32 v244, 0x24400, v2
	v_readlane_b32 s26, v254, 62
	v_readlane_b32 s49, v255, 3
	v_readlane_b32 s48, v255, 1
	s_mov_b32 s50, 0
	s_barrier
	s_branch .LBB0_1216

; #define PG8_STAGE(bufoff, RS, soff, voff) do { _Pragma("unroll") for (int _i = 0; _i < 2; ++_i) \
;         __builtin_amdgcn_raw_ptr_buffer_load_lds(RS, (PG8_LAS void*)(lds + (bufoff) + sgpr_opaque(ldsw) + _i * 8192), 16, (int)(voff)[_i], (int)(soff), 0, 0); } while (0)
; #define PG8_LDA(dst, b, h) do { _Pragma("unroll") for (int m = 0; m < 4; ++m) _Pragma("unroll") for (int k = 0; k < 2; ++k) dst[m][k] = *(const PG8_LAS f16x8*)(lds + PG8_SA(b, h) + aoff + m * 2048 + k * 1024); } while (0)
; #define PG8_WAIT_L(n) asm volatile("s_waitcnt lgkmcnt(" #n ")" ::: "memory")
; #define PG8_BAR __builtin_amdgcn_s_barrier()
; #define PG8_SCHED __builtin_amdgcn_sched_barrier(0)
; template <class Epi, class Sched, bool ALIGN_EPI = false, bool SP2 = false, bool I8 = false, bool ATILED = false>
; __device__ __forceinline__ void gemm_phase(PG8_LAS unsigned char* lds, const Gemm g, const Sched& S, const Epi& E, const int wid) {
;     ...
;             PG8_WAIT_VG; PG8_WAIT_L(0); PG8_BAR; PG8_MMA(0, 0, At, B0); PG8_MMA(0, 1, At, B1); PG8_BAR; PG8_SCHED;
;             PG8_LDA(At, 0, 1); PG8_STAGE(PG8_SB(0, 0), rsB, b2, voffB); PG8_STAGE(PG8_SB(0, 1), rsB, b2 + hstep, voffB); PG8_STAGE(PG8_SA(0, 0), rsA, a2, voffA);
.Lgr8:
	s_waitcnt vmcnt(36)
	s_waitcnt lgkmcnt(0)
	s_barrier
	s_setprio 1
	s_waitcnt lgkmcnt(7)
	v_mfma_i32_16x16x64_i8 v[182:185], v[26:29], v[58:61], v[182:185]
	v_mfma_i32_16x16x64_i8 v[178:181], v[34:37], v[58:61], v[178:181]
	s_waitcnt lgkmcnt(5)
	v_mfma_i32_16x16x64_i8 v[158:161], v[26:29], v[66:69], v[158:161]
	v_mfma_i32_16x16x64_i8 v[154:157], v[34:37], v[66:69], v[154:157]
	s_waitcnt lgkmcnt(3)
	v_mfma_i32_16x16x64_i8 v[142:145], v[26:29], v[162:165], v[142:145]
	v_mfma_i32_16x16x64_i8 v[138:141], v[34:37], v[162:165], v[138:141]
	s_waitcnt lgkmcnt(1)
	v_mfma_i32_16x16x64_i8 v[126:129], v[26:29], v[186:189], v[126:129]
	v_mfma_i32_16x16x64_i8 v[122:125], v[34:37], v[186:189], v[122:125]
	v_mfma_i32_16x16x64_i8 v[182:185], v[30:33], v[62:65], v[182:185]
	v_mfma_i32_16x16x64_i8 v[178:181], v[38:41], v[62:65], v[178:181]
	v_mfma_i32_16x16x64_i8 v[158:161], v[30:33], v[70:73], v[158:161]
	v_mfma_i32_16x16x64_i8 v[154:157], v[38:41], v[70:73], v[154:157]
	v_mfma_i32_16x16x64_i8 v[142:145], v[30:33], v[174:177], v[142:145]
	v_mfma_i32_16x16x64_i8 v[138:141], v[38:41], v[174:177], v[138:141]
	s_waitcnt lgkmcnt(0)
	v_mfma_i32_16x16x64_i8 v[126:129], v[30:33], v[190:193], v[126:129]
	v_mfma_i32_16x16x64_i8 v[122:125], v[38:41], v[190:193], v[122:125]
	s_setprio 0
	s_setprio 1
	v_mfma_i32_16x16x64_i8 v[170:173], v[42:45], v[58:61], v[170:173]
	v_mfma_i32_16x16x64_i8 v[58:61], v[50:53], v[58:61], v[166:169]
	v_mfma_i32_16x16x64_i8 v[170:173], v[46:49], v[62:65], v[170:173]
	v_mfma_i32_16x16x64_i8 v[58:61], v[54:57], v[62:65], v[58:61]
	v_mfma_i32_16x16x64_i8 v[62:65], v[42:45], v[66:69], v[150:153]
	v_mfma_i32_16x16x64_i8 v[66:69], v[50:53], v[66:69], v[146:149]
	v_mfma_i32_16x16x64_i8 v[130:133], v[50:53], v[162:165], v[130:133]
	v_mfma_i32_16x16x64_i8 v[118:121], v[42:45], v[186:189], v[118:121]
	v_mfma_i32_16x16x64_i8 v[114:117], v[50:53], v[186:189], v[114:117]
	v_mfma_i32_16x16x64_i8 v[62:65], v[46:49], v[70:73], v[62:65]
	v_mfma_i32_16x16x64_i8 v[66:69], v[54:57], v[70:73], v[66:69]
	v_mfma_i32_16x16x64_i8 v[70:73], v[42:45], v[162:165], v[134:137]
	v_mfma_i32_16x16x64_i8 v[130:133], v[54:57], v[174:177], v[130:133]
	v_mfma_i32_16x16x64_i8 v[118:121], v[46:49], v[190:193], v[118:121]
	v_mfma_i32_16x16x64_i8 v[114:117], v[54:57], v[190:193], v[114:117]
	v_mfma_i32_16x16x64_i8 v[70:73], v[46:49], v[174:177], v[70:73]
	s_setprio 0
	s_barrier
	s_mov_b32 s62, s85
	ds_read_b128 v[134:137], v209 offset:16384
	ds_read_b128 v[146:149], v209 offset:17408
	ds_read_b128 v[150:153], v209 offset:18432
	ds_read_b128 v[162:165], v209 offset:19456
	ds_read_b128 v[166:169], v209 offset:20480
	ds_read_b128 v[174:177], v209 offset:21504
	ds_read_b128 v[186:189], v209 offset:22528
	ds_read_b128 v[190:193], v209 offset:23552
	s_lshl1_add_u32 m0, s85, 0x10000
	s_mov_b32 s62, s85
	buffer_load_dwordx4 v194, s[64:67], s52 offen lds
	s_mov_b32 s63, s85
	buffer_load_dwordx4 v194, s[64:67], s52 offen offset:1024 lds
	s_add_i32 s62, s52, 0x4000
	s_lshl1_add_u32 m0, s85, 0x14000
	s_mov_b32 s63, s85
	buffer_load_dwordx4 v194, s[64:67], s62 offen lds
	s_nop 0
	buffer_load_dwordx4 v194, s[64:67], s62 offen offset:1024 lds
	s_mov_b32 s62, s85
	s_mov_b32 m0, s62
	s_mov_b32 s62, s85
	buffer_load_dwordx4 v0, s[88:91], s69 offen lds
	s_add_i32 m0, s62, 0x2000
	s_nop 0
	buffer_load_dwordx4 v195, s[88:91], s69 offen lds
	s_cmp_lg_u32 s61, 0
	s_cbranch_scc1 .Lgr9
	s_waitcnt vmcnt(8)

; #define PG8_STAGE(bufoff, RS, soff, voff) do { _Pragma("unroll") for (int _i = 0; _i < 2; ++_i) \
;         __builtin_amdgcn_raw_ptr_buffer_load_lds(RS, (PG8_LAS void*)(lds + (bufoff) + sgpr_opaque(ldsw) + _i * 8192), 16, (int)(voff)[_i], (int)(soff), 0, 0); } while (0)
; #define PG8_LDA(dst, b, h) do { _Pragma("unroll") for (int m = 0; m < 4; ++m) _Pragma("unroll") for (int k = 0; k < 2; ++k) dst[m][k] = *(const PG8_LAS f16x8*)(lds + PG8_SA(b, h) + aoff + m * 2048 + k * 1024); } while (0)
; #define PG8_WAIT_L(n) asm volatile("s_waitcnt lgkmcnt(" #n ")" ::: "memory")
; #define PG8_BAR __builtin_amdgcn_s_barrier()
; #define PG8_SCHED __builtin_amdgcn_sched_barrier(0)
; template <class Epi, class Sched, bool ALIGN_EPI = false, bool SP2 = false, bool I8 = false, bool ATILED = false>
; __device__ __forceinline__ void gemm_phase(PG8_LAS unsigned char* lds, const Gemm g, const Sched& S, const Epi& E, const int wid) {
;     ...
;             PG8_WAIT_VG; PG8_WAIT_L(0); PG8_BAR; PG8_MMA(0, 0, At, B0); PG8_MMA(0, 1, At, B1); PG8_BAR; PG8_SCHED;
;             PG8_LDA(At, 1, 1); PG8_STAGE(PG8_SB(1, 0), rsB, b3, voffB); PG8_STAGE(PG8_SB(1, 1), rsB, b3 + hstep, voffB); PG8_STAGE(PG8_SA(1, 0), rsA, a3, voffA);
.Lgr10:
	s_waitcnt vmcnt(36)
	s_waitcnt lgkmcnt(0)
	s_barrier
	s_setprio 1
	s_waitcnt lgkmcnt(7)
	v_mfma_i32_16x16x64_i8 v[134:137], v[42:45], v[82:85], v[182:185]
	s_waitcnt lgkmcnt(6)
	v_mfma_i32_16x16x64_i8 v[182:185], v[46:49], v[86:89], v[134:137]
	v_mfma_i32_16x16x64_i8 v[134:137], v[50:53], v[82:85], v[178:181]
	v_mfma_i32_16x16x64_i8 v[178:181], v[54:57], v[86:89], v[134:137]
	s_waitcnt lgkmcnt(5)
	v_mfma_i32_16x16x64_i8 v[134:137], v[42:45], v[98:101], v[158:161]
	s_waitcnt lgkmcnt(4)
	v_mfma_i32_16x16x64_i8 v[158:161], v[46:49], v[102:105], v[134:137]
	v_mfma_i32_16x16x64_i8 v[134:137], v[50:53], v[98:101], v[154:157]
	v_mfma_i32_16x16x64_i8 v[154:157], v[54:57], v[102:105], v[134:137]
	s_waitcnt lgkmcnt(3)
	v_mfma_i32_16x16x64_i8 v[134:137], v[42:45], v[212:215], v[142:145]
	s_waitcnt lgkmcnt(2)
	v_mfma_i32_16x16x64_i8 v[142:145], v[46:49], v[216:219], v[134:137]
	v_mfma_i32_16x16x64_i8 v[134:137], v[50:53], v[212:215], v[138:141]
	s_waitcnt lgkmcnt(1)
	v_mfma_i32_16x16x64_i8 v[126:129], v[42:45], v[220:223], v[126:129]
	v_mfma_i32_16x16x64_i8 v[122:125], v[50:53], v[220:223], v[122:125]
	v_mfma_i32_16x16x64_i8 v[138:141], v[54:57], v[216:219], v[134:137]
	s_waitcnt lgkmcnt(0)
	v_mfma_i32_16x16x64_i8 v[126:129], v[46:49], v[224:227], v[126:129]
	v_mfma_i32_16x16x64_i8 v[122:125], v[54:57], v[224:227], v[122:125]
	s_setprio 0
	s_setprio 1
	v_mfma_i32_16x16x64_i8 v[58:61], v[186:189], v[82:85], v[58:61]
	v_mfma_i32_16x16x64_i8 v[166:169], v[190:193], v[86:89], v[58:61]
	v_mfma_i32_16x16x64_i8 v[58:61], v[162:165], v[98:101], v[62:65]
	v_mfma_i32_16x16x64_i8 v[150:153], v[174:177], v[102:105], v[58:61]
	v_mfma_i32_16x16x64_i8 v[58:61], v[186:189], v[98:101], v[66:69]
	v_mfma_i32_16x16x64_i8 v[134:137], v[162:165], v[82:85], v[170:173]
	v_mfma_i32_16x16x64_i8 v[146:149], v[190:193], v[102:105], v[58:61]
	v_mfma_i32_16x16x64_i8 v[58:61], v[162:165], v[212:215], v[70:73]
	v_mfma_i32_16x16x64_i8 v[170:173], v[174:177], v[86:89], v[134:137]
	v_mfma_i32_16x16x64_i8 v[134:137], v[174:177], v[216:219], v[58:61]
	v_mfma_i32_16x16x64_i8 v[58:61], v[186:189], v[212:215], v[130:133]
	v_mfma_i32_16x16x64_i8 v[130:133], v[190:193], v[216:219], v[58:61]
	v_mfma_i32_16x16x64_i8 v[58:61], v[162:165], v[220:223], v[118:121]
	v_mfma_i32_16x16x64_i8 v[118:121], v[174:177], v[224:227], v[58:61]
	v_mfma_i32_16x16x64_i8 v[58:61], v[186:189], v[220:223], v[114:117]
	v_mfma_i32_16x16x64_i8 v[114:117], v[190:193], v[224:227], v[58:61]
	s_setprio 0
	s_barrier
	s_mov_b32 s62, s85
	s_nop 3
	ds_read_b128 v[58:61], v209 offset:49152
	ds_read_b128 v[62:65], v209 offset:50176
	ds_read_b128 v[66:69], v209 offset:51200
	ds_read_b128 v[70:73], v209 offset:52224
	ds_read_b128 v[212:215], v209 offset:53248
	ds_read_b128 v[216:219], v209 offset:54272
	ds_read_b128 v[220:223], v209 offset:55296
	ds_read_b128 v[224:227], v209 offset:56320
	s_lshl1_add_u32 m0, s85, 0x18000
	s_mov_b32 s62, s85
	buffer_load_dwordx4 v194, s[64:67], s53 offen lds
	s_add_i32 s52, s52, 0xc000
	buffer_load_dwordx4 v194, s[64:67], s53 offen offset:1024 lds
	s_mov_b32 s53, s85
	s_lshl1_add_u32 m0, s85, 0x1c000
	s_mov_b32 s53, s85
	buffer_load_dwordx4 v194, s[64:67], s52 offen lds
	s_nop 0
	buffer_load_dwordx4 v194, s[64:67], s52 offen offset:1024 lds
	s_mov_b32 s52, s85
	s_add_i32 m0, s52, 0x8000
	s_mov_b32 s52, s85
	buffer_load_dwordx4 v0, s[88:91], s51 offen lds
	s_add_i32 m0, s52, 0xa000
	s_nop 0
	buffer_load_dwordx4 v195, s[88:91], s51 offen lds
	s_cmp_lg_u32 s61, 0
	s_cbranch_scc1 .Lgr11
	s_waitcnt vmcnt(8)

;     __host__ __device__ bool next(int i, Unit& u) const { if (!so.next(i / 3, u)) return false; u.pn += 4 * (i % 3); u.idx = i; return true; }
; #define PG8_BAR __builtin_amdgcn_s_barrier()
; template <class Epi, class Sched, bool ALIGN_EPI = false, bool SP2 = false, bool I8 = false, bool ATILED = false>
; __device__ __forceinline__ void gemm_phase(PG8_LAS unsigned char* lds, const Gemm g, const Sched& S, const Epi& E, const int wid) {
;     ...
;     for (int i = 0; i < 2; ++i) { int R, C; stage_rc(tid * 16 + i * 8192, R, C); const int Rb = Epi::PERM ? ((R & ~31) + perm32(R & 31)) : R;
;         voffA[i] = (unsigned)(R * (ATILED ? BK : K) + C) * 2u; voffB[i] = (unsigned)(Rb * K + C) * 2u; }
;     const unsigned kstep = (unsigned)(BK * 2);
;     const unsigned hstep = (unsigned)HALF * K * 2;
;     const unsigned tstep = 2 * hstep;
;     const unsigned kstepA = ATILED ? (unsigned)(BM * BK * 2) : kstep, hstepA = ATILED ? (unsigned)(HALF * BK * 2) : hstep, tstepA = ATILED ? (unsigned)nt * (unsigned)(BM * BK * 2) : tstep;
;     const __amdgpu_buffer_rsrc_t rsA = __builtin_amdgcn_make_buffer_rsrc((void*)g.A, 0, 0x7fffffff, 0x00020000), rsB = __builtin_amdgcn_make_buffer_rsrc((void*)g.Bt, 0, 0x7fffffff, 0x00020000);
;     const unsigned ldsw = (unsigned)wid * 1024u;
;     const int aoff = lds_byte(wr * 64 + fr, fq * 8), boff = lds_byte(wc * 32 + fr, fq * 8);
;     ...
;     Unit cur, nxt; int ui = 0;
;     if (!S.next(0, cur)) return;
;     f32x4 acc[2][2][4][2];
; #pragma unroll
;     for (int a = 0; a < 2; ++a)
; #pragma unroll
;         for (int b = 0; b < 2; ++b)
; #pragma unroll
;             for (int m = 0; m < 4; ++m)
; #pragma unroll
;                 for (int n = 0; n < 2; ++n) acc[a][b][m][n] = (f32x4){0.f, 0.f, 0.f, 0.f};
;     f16x8 At[4][2], B0[2][2], B1[2][2];
;     unsigned cA = (unsigned)cur.pm * tstepA + (unsigned)(cur.pm >> 4) * g.gapA, cB = (unsigned)cur.pn * tstep;
;     S.a_ready(cur);
;     if constexpr (SP2) {
;         PG8_STAGE(PG8_SB(0, 0), rsB, cB, voffB); PG8_STAGE(PG8_SB(0, 1), rsB, cB + hstep, voffB); PG8_STAGE(PG8_SA(0, 0), rsA, cA, voffA); PG8_STAGE(PG8_SA(0, 1), rsA, cA + hstepA, voffA);
;         if (wr == 1) PG8_BAR;
;         PG8_WAIT_V(2); PG8_BAR;
;         PG8_STAGE(PG8_SB(1, 0), rsB, cB + kstep, voffB); PG8_STAGE(PG8_SA(1, 0), rsA, cA + kstepA, voffA); PG8_STAGE(PG8_SB(1, 1), rsB, cB + hstep + kstep, voffB);
;         PG8_WAIT_V(6); PG8_BAR;
.LBB0_1598:
	v_readlane_b32 s26, v254, 20
	v_readlane_b32 s27, v254, 21
	s_andn2_b64 vcc, exec, s[26:27]
	s_waitcnt lgkmcnt(0)
	s_barrier
	v_mbcnt_lo_u32_b32 v0, -1, 0
	v_mbcnt_hi_u32_b32 v0, -1, v0
	s_cbranch_vccnz .LBB0_1618
	v_lshl_add_u32 v2, v0, 4, s85
	v_ashrrev_i32_e32 v3, 31, v2
	v_lshrrev_b32_e32 v3, 22, v3
	v_add_u32_e32 v3, v2, v3
	v_ashrrev_i32_e32 v3, 10, v3
	s_waitcnt vmcnt(0)
	v_mul_i32_i24_e32 v4, 0x400, v3
	v_sub_u32_e32 v4, v2, v4
	v_lshrrev_b32_e32 v5, 4, v4
	v_bitop3_b32 v4, v5, v4, 32 bitop3:0x6c
	s_ashr_i32 s49, s48, 31
	v_ashrrev_i32_e32 v6, 31, v4
	s_lshl_b64 s[26:27], s[48:49], 22
	v_lshrrev_b32_e32 v6, 26, v6
	s_add_u32 s26, s46, s26
	v_lshlrev_b32_e32 v5, 3, v3
	v_add_u32_e32 v6, v4, v6
	s_addc_u32 s27, s47, s27
	v_and_b32_e32 v5, -16, v5
	v_ashrrev_i32_e32 v7, 6, v6
	v_and_b32_e32 v6, 0xc0, v6
	s_add_u32 s64, s26, 0x1f700000
	v_add_u32_e32 v5, v7, v5
	v_sub_u32_e32 v4, v4, v6
	s_addc_u32 s26, s27, 0
	v_lshlrev_b32_e32 v3, 5, v3
	v_ashrrev_i16_sdwa v4, v232, sext(v4) dst_sel:DWORD dst_unused:UNUSED_PAD src0_sel:DWORD src1_sel:BYTE_0
	v_lshlrev_b32_e32 v6, 1, v5
	v_lshrrev_b32_e32 v8, 2, v5
	v_and_b32_e32 v7, 3, v7
	s_mov_b32 s27, 0x3fffe0
	v_and_b32_e32 v3, 32, v3
	v_bfe_i32 v4, v4, 0, 16
	v_and_b32_e32 v6, 24, v6
	v_and_b32_e32 v8, 4, v8
	v_and_or_b32 v7, v5, s27, v7
	v_or3_b32 v6, v7, v8, v6
	v_add_lshl_u32 v3, v3, v4, 1
	v_add_u32_e32 v2, 0x2000, v2
	v_lshl_add_u32 v172, v5, 10, v3
	v_mbcnt_lo_u32_b32 v173, -1, 0
	v_mbcnt_hi_u32_b32 v173, -1, v173
	s_lshl_b32 s100, s85, 1
	v_lshl_add_u32 v173, v173, 4, s100
	v_ashrrev_i32_e32 v3, 31, v2
	v_lshrrev_b32_e32 v3, 22, v3
	v_add_u32_e32 v3, v2, v3
	v_ashrrev_i32_e32 v3, 10, v3
	v_mul_i32_i24_e32 v4, 0x400, v3
	v_sub_u32_e32 v2, v2, v4
	v_lshrrev_b32_e32 v4, 4, v2
	v_bitop3_b32 v2, v4, v2, 32 bitop3:0x6c
	v_ashrrev_i32_e32 v5, 31, v2
	v_lshrrev_b32_e32 v5, 26, v5
	v_add_u32_e32 v5, v2, v5
	v_ashrrev_i32_e32 v6, 6, v5
	v_and_b32_e32 v5, 0xffc0, v5
	v_sub_u32_e32 v2, v2, v5
	v_lshlrev_b32_e32 v4, 3, v3
	v_lshrrev_b16_e32 v5, 7, v2
	v_and_b32_e32 v4, -16, v4
	v_and_b32_e32 v5, 1, v5
	v_add_u32_e32 v4, v6, v4
	v_add_u16_e32 v2, v2, v5
	s_and_b32 s65, s26, 0xffff
	s_mov_b32 s26, s85
	v_lshlrev_b32_e32 v3, 5, v3
	v_ashrrev_i16_sdwa v2, v232, sext(v2) dst_sel:DWORD dst_unused:UNUSED_PAD src0_sel:DWORD src1_sel:BYTE_0
	v_lshlrev_b32_e32 v5, 1, v4
	v_lshrrev_b32_e32 v7, 2, v4
	v_and_b32_e32 v6, 3, v6
	v_and_b32_e32 v3, 32, v3
	v_bfe_i32 v2, v2, 0, 16
	v_and_b32_e32 v5, 24, v5
	v_and_b32_e32 v7, 4, v7
	v_and_or_b32 v6, v4, s27, v6
	s_lshl1_add_u32 m0, s85, 0x10000
	v_readlane_b32 s27, v254, 51
	s_bfe_u32 s100, s27, 0x10011
	s_bfe_u32 s101, s27, 0x10007
	s_and_b32 s27, s27, 0xfffc0000
	s_lshl_b32 s100, s100, 14
	s_lshl_b32 s101, s101, 15
	s_or_b32 s27, s27, s100
	s_or_b32 s27, s27, s101
	s_mov_b32 s26, s85
	v_or3_b32 v5, v6, v7, v5
	v_add_lshl_u32 v2, v3, v2, 1
	v_mbcnt_lo_u32_b32 v175, -1, 0
	v_mbcnt_hi_u32_b32 v175, -1, v175
	v_lshl_add_u32 v175, v175, 4, s85
	v_add_u32_e32 v175, 0x2000, v175
	s_mov_b32 s90, s66
	buffer_load_dwordx4 v173, s[64:67], s27 offen lds
	s_mov_b32 s26, s85
	buffer_load_dwordx4 v173, s[64:67], s27 offen offset:1024 lds
	s_lshl1_add_u32 m0, s85, 0x14000
	v_readlane_b32 s27, v254, 45
	s_bfe_u32 s100, s27, 0x10011
	s_bfe_u32 s101, s27, 0x10007
	s_and_b32 s27, s27, 0xfffc0000
	s_lshl_b32 s100, s100, 14
	s_lshl_b32 s101, s101, 15
	s_or_b32 s27, s27, s100
	s_or_b32 s27, s27, s101
	s_mov_b32 s26, s85
	s_mov_b32 s91, s67
	v_lshl_add_u32 v174, v4, 10, v2
	v_readlane_b32 s22, v253, 31
	v_readlane_b32 s23, v253, 32
	buffer_load_dwordx4 v173, s[64:67], s27 offen lds
	s_mov_b32 s26, s85
	buffer_load_dwordx4 v173, s[64:67], s27 offen offset:1024 lds
	s_mov_b32 m0, s26
	v_readlane_b32 s27, v254, 49
	s_mov_b32 s26, s85
	s_and_b64 vcc, exec, s[22:23]
	s_nop 2
	buffer_load_dwordx4 v172, s[88:91], s27 offen lds
	s_add_i32 m0, s26, 0x2000
	s_mov_b32 s26, s85
	buffer_load_dwordx4 v174, s[88:91], s27 offen lds
	s_add_i32 m0, s26, 0x4000
	v_readlane_b32 s27, v254, 47
	s_mov_b32 s26, s85
	s_nop 3
	buffer_load_dwordx4 v172, s[88:91], s27 offen lds
	s_add_i32 m0, s26, 0x6000
	s_nop 0
	buffer_load_dwordx4 v174, s[88:91], s27 offen lds
	s_cbranch_vccnz .LBB0_1601
	s_barrier
.LBB0_1601:
	s_mov_b32 s26, s85
	s_add_u32 s36, s44, 0xe800000
	s_waitcnt vmcnt(2)
	s_barrier
	s_addc_u32 s37, s45, 0
	s_lshl1_add_u32 m0, s85, 0x18000
	v_readlane_b32 s27, v254, 48
	s_bfe_u32 s100, s27, 0x10011
	s_bfe_u32 s101, s27, 0x10007
	s_and_b32 s27, s27, 0xfffc0000
	s_lshl_b32 s100, s100, 14
	s_lshl_b32 s101, s101, 15
	s_or_b32 s27, s27, s100
	s_or_b32 s27, s27, s101
	s_mov_b32 s26, s85
	v_and_b32_e32 v176, 15, v0
	v_or_b32_e32 v177, s96, v176
	v_lshlrev_b32_e32 v4, 6, v177
	v_and_b32_e32 v5, 48, v0
	buffer_load_dwordx4 v173, s[64:67], s27 offen lds
	s_mov_b32 s26, s85
	buffer_load_dwordx4 v173, s[64:67], s27 offen offset:1024 lds
	s_add_i32 m0, s26, 0x8000
	v_readlane_b32 s27, v254, 50
	s_mov_b32 s26, s85
	v_ashrrev_i32_e32 v3, 6, v0
	v_ashrrev_i32_e32 v2, 1, v0
	v_lshlrev_b32_e32 v7, 2, v177
	v_and_b32_e32 v2, -8, v2
	buffer_load_dwordx4 v172, s[88:91], s27 offen lds
	s_add_i32 m0, s26, 0xa000
	s_mov_b32 s26, s85
	buffer_load_dwordx4 v174, s[88:91], s27 offen lds
	s_lshl1_add_u32 m0, s85, 0x1c000
	v_readlane_b32 s27, v254, 52
	s_bfe_u32 s100, s27, 0x10011
	s_bfe_u32 s101, s27, 0x10007
	s_and_b32 s27, s27, 0xfffc0000
	s_lshl_b32 s100, s100, 14
	s_lshl_b32 s101, s101, 15
	s_or_b32 s27, s27, s100
	s_or_b32 s27, s27, s101
	s_mov_b32 s26, s85
	v_and_b32_e32 v7, 32, v7
	v_lshlrev_b32_e32 v0, 2, v0
	v_and_b32_e32 v0, 32, v0
	s_mov_b32 s46, 0
	buffer_load_dwordx4 v173, s[64:67], s27 offen lds
	s_movk_i32 s26, 0x3c0
	buffer_load_dwordx4 v173, s[64:67], s27 offen offset:1024 lds
	v_and_or_b32 v4, v4, s26, v5
	v_readlane_b32 s26, v253, 60
	s_waitcnt vmcnt(6)
	v_readlane_b32 s44, v254, 44
	v_readlane_b32 s45, v254, 46
	v_lshl_add_u32 v6, v3, 10, s26
	v_readlane_b32 s26, v253, 62
	v_bitop3_b32 v178, v4, v6, v7 bitop3:0xde
	v_lshl_or_b32 v4, v176, 6, v5
	v_add_lshl_u32 v3, v3, s26, 10
	v_readlane_b32 s26, v253, 61
	v_bitop3_b32 v179, v4, v3, v0 bitop3:0xde
	v_readlane_b32 s50, v254, 51
	v_add_u32_e32 v180, s26, v2
	v_lshlrev_b32_e32 v0, 2, v180
	v_add_u32_e32 v181, 0x22400, v0
	v_add_u32_e32 v182, 0x24400, v0
	v_lshlrev_b32_e32 v0, 7, v177
	v_and_b32_e32 v2, 56, v180
	v_and_b32_e32 v0, 0x6780, v0
	v_lshl_add_u64 v[162:163], s[36:37], 0, v[0:1]
	v_lshlrev_b32_e32 v0, 1, v2
	v_readlane_b32 s49, v254, 49
	s_mov_b32 s51, 0
	s_barrier
	s_branch .LBB0_1604

; #define PG8_STAGE(bufoff, RS, soff, voff) do { _Pragma("unroll") for (int _i = 0; _i < 2; ++_i) \
;         __builtin_amdgcn_raw_ptr_buffer_load_lds(RS, (PG8_LAS void*)(lds + (bufoff) + sgpr_opaque(ldsw) + _i * 8192), 16, (int)(voff)[_i], (int)(soff), 0, 0); } while (0)
; #define PG8_LDA(dst, b, h) do { _Pragma("unroll") for (int m = 0; m < 4; ++m) _Pragma("unroll") for (int k = 0; k < 2; ++k) dst[m][k] = *(const PG8_LAS f16x8*)(lds + PG8_SA(b, h) + aoff + m * 2048 + k * 1024); } while (0)
; #define PG8_WAIT_L(n) asm volatile("s_waitcnt lgkmcnt(" #n ")" ::: "memory")
; #define PG8_BAR __builtin_amdgcn_s_barrier()
; #define PG8_SCHED __builtin_amdgcn_sched_barrier(0)
; template <class Epi, class Sched, bool ALIGN_EPI = false, bool SP2 = false, bool I8 = false, bool ATILED = false>
; __device__ __forceinline__ void gemm_phase(PG8_LAS unsigned char* lds, const Gemm g, const Sched& S, const Epi& E, const int wid) {
;     ...
;             PG8_WAIT_VG; PG8_WAIT_L(0); PG8_BAR; PG8_MMA(0, 0, At, B0); PG8_MMA(0, 1, At, B1); PG8_BAR; PG8_SCHED;
;             PG8_LDA(At, 0, 1); PG8_STAGE(PG8_SB(0, 0), rsB, b2, voffB); PG8_STAGE(PG8_SB(0, 1), rsB, b2 + hstep, voffB); PG8_STAGE(PG8_SA(0, 0), rsA, a2, voffA);
.Lgr16:
	s_waitcnt vmcnt(24)
	s_waitcnt lgkmcnt(0)
	s_barrier
	s_setprio 1
	s_waitcnt lgkmcnt(7)
	v_mfma_i32_16x16x64_i8 v[158:161], v[106:109], v[164:167], v[158:161]
	v_mfma_i32_16x16x64_i8 v[154:157], v[114:117], v[164:167], v[154:157]
	s_waitcnt lgkmcnt(5)
	v_mfma_i32_16x16x64_i8 v[134:137], v[106:109], v[184:187], v[134:137]
	v_mfma_i32_16x16x64_i8 v[122:125], v[114:117], v[184:187], v[122:125]
	s_waitcnt lgkmcnt(3)
	v_mfma_i32_16x16x64_i8 v[94:97], v[106:109], v[192:195], v[94:97]
	v_mfma_i32_16x16x64_i8 v[90:93], v[114:117], v[192:195], v[90:93]
	s_waitcnt lgkmcnt(1)
	v_mfma_i32_16x16x64_i8 v[78:81], v[106:109], v[212:215], v[78:81]
	v_mfma_i32_16x16x64_i8 v[74:77], v[114:117], v[212:215], v[74:77]
	v_mfma_i32_16x16x64_i8 v[158:161], v[110:113], v[168:171], v[158:161]
	v_mfma_i32_16x16x64_i8 v[154:157], v[118:121], v[168:171], v[154:157]
	v_mfma_i32_16x16x64_i8 v[134:137], v[110:113], v[188:191], v[134:137]
	v_mfma_i32_16x16x64_i8 v[122:125], v[118:121], v[188:191], v[122:125]
	v_mfma_i32_16x16x64_i8 v[94:97], v[110:113], v[208:211], v[94:97]
	v_mfma_i32_16x16x64_i8 v[90:93], v[118:121], v[208:211], v[90:93]
	s_waitcnt lgkmcnt(0)
	v_mfma_i32_16x16x64_i8 v[78:81], v[110:113], v[216:219], v[78:81]
	v_mfma_i32_16x16x64_i8 v[74:77], v[118:121], v[216:219], v[74:77]
	s_setprio 0
	s_setprio 1
	v_mfma_i32_16x16x64_i8 v[150:153], v[126:129], v[164:167], v[150:153]
	v_mfma_i32_16x16x64_i8 v[146:149], v[138:141], v[164:167], v[146:149]
	v_mfma_i32_16x16x64_i8 v[102:105], v[126:129], v[184:187], v[102:105]
	v_mfma_i32_16x16x64_i8 v[98:101], v[138:141], v[184:187], v[98:101]
	v_mfma_i32_16x16x64_i8 v[86:89], v[126:129], v[192:195], v[86:89]
	v_mfma_i32_16x16x64_i8 v[82:85], v[138:141], v[192:195], v[82:85]
	v_mfma_i32_16x16x64_i8 v[70:73], v[126:129], v[212:215], v[70:73]
	v_mfma_i32_16x16x64_i8 v[66:69], v[138:141], v[212:215], v[66:69]
	v_mfma_i32_16x16x64_i8 v[150:153], v[130:133], v[168:171], v[150:153]
	v_mfma_i32_16x16x64_i8 v[146:149], v[142:145], v[168:171], v[146:149]
	v_mfma_i32_16x16x64_i8 v[102:105], v[130:133], v[188:191], v[102:105]
	v_mfma_i32_16x16x64_i8 v[98:101], v[142:145], v[188:191], v[98:101]
	v_mfma_i32_16x16x64_i8 v[86:89], v[130:133], v[208:211], v[86:89]
	v_mfma_i32_16x16x64_i8 v[82:85], v[142:145], v[208:211], v[82:85]
	v_mfma_i32_16x16x64_i8 v[70:73], v[130:133], v[216:219], v[70:73]
	v_mfma_i32_16x16x64_i8 v[66:69], v[142:145], v[216:219], v[66:69]
	s_setprio 0
	s_barrier
	s_mov_b32 s59, s85
	ds_read_b128 v[164:167], v178 offset:16384
	ds_read_b128 v[168:171], v178 offset:17408
	ds_read_b128 v[184:187], v178 offset:18432
	ds_read_b128 v[188:191], v178 offset:19456
	ds_read_b128 v[192:195], v178 offset:20480
	ds_read_b128 v[208:211], v178 offset:21504
	ds_read_b128 v[212:215], v178 offset:22528
	ds_read_b128 v[216:219], v178 offset:23552
	s_lshl1_add_u32 m0, s85, 0x10000
	s_mov_b32 s59, s85
	buffer_load_dwordx4 v173, s[64:67], s53 offen lds
	s_mov_b32 s60, s85
	buffer_load_dwordx4 v173, s[64:67], s53 offen offset:1024 lds
	s_add_i32 s59, s53, 0x4000
	s_lshl1_add_u32 m0, s85, 0x14000
	s_mov_b32 s60, s85
	buffer_load_dwordx4 v173, s[64:67], s59 offen lds
	s_nop 0
	buffer_load_dwordx4 v173, s[64:67], s59 offen offset:1024 lds
	s_mov_b32 s59, s85
	s_mov_b32 m0, s59
	s_mov_b32 s59, s85
	buffer_load_dwordx4 v172, s[88:91], s58 offen lds
	s_add_i32 m0, s59, 0x2000
	s_nop 0
	buffer_load_dwordx4 v174, s[88:91], s58 offen lds
	s_cmp_lg_u32 s55, 0
	s_cbranch_scc1 .Lgr17
	s_waitcnt vmcnt(8)

; #define PG8_STAGE(bufoff, RS, soff, voff) do { _Pragma("unroll") for (int _i = 0; _i < 2; ++_i) \
;         __builtin_amdgcn_raw_ptr_buffer_load_lds(RS, (PG8_LAS void*)(lds + (bufoff) + sgpr_opaque(ldsw) + _i * 8192), 16, (int)(voff)[_i], (int)(soff), 0, 0); } while (0)
; #define PG8_LDA(dst, b, h) do { _Pragma("unroll") for (int m = 0; m < 4; ++m) _Pragma("unroll") for (int k = 0; k < 2; ++k) dst[m][k] = *(const PG8_LAS f16x8*)(lds + PG8_SA(b, h) + aoff + m * 2048 + k * 1024); } while (0)
; #define PG8_WAIT_L(n) asm volatile("s_waitcnt lgkmcnt(" #n ")" ::: "memory")
; #define PG8_BAR __builtin_amdgcn_s_barrier()
; #define PG8_SCHED __builtin_amdgcn_sched_barrier(0)
; template <class Epi, class Sched, bool ALIGN_EPI = false, bool SP2 = false, bool I8 = false, bool ATILED = false>
; __device__ __forceinline__ void gemm_phase(PG8_LAS unsigned char* lds, const Gemm g, const Sched& S, const Epi& E, const int wid) {
;     ...
;             PG8_WAIT_VG; PG8_WAIT_L(0); PG8_BAR; PG8_MMA(0, 0, At, B0); PG8_MMA(0, 1, At, B1); PG8_BAR; PG8_SCHED;
;             PG8_LDA(At, 1, 1); PG8_STAGE(PG8_SB(1, 0), rsB, b3, voffB); PG8_STAGE(PG8_SB(1, 1), rsB, b3 + hstep, voffB); PG8_STAGE(PG8_SA(1, 0), rsA, a3, voffA);
.Lgr18:
	s_waitcnt vmcnt(24)
	s_waitcnt lgkmcnt(0)
	s_barrier
	s_setprio 1
	s_waitcnt lgkmcnt(7)
	v_mfma_i32_16x16x64_i8 v[158:161], v[106:109], v[164:167], v[158:161]
	v_mfma_i32_16x16x64_i8 v[154:157], v[114:117], v[164:167], v[154:157]
	s_waitcnt lgkmcnt(5)
	v_mfma_i32_16x16x64_i8 v[134:137], v[106:109], v[184:187], v[134:137]
	v_mfma_i32_16x16x64_i8 v[122:125], v[114:117], v[184:187], v[122:125]
	s_waitcnt lgkmcnt(3)
	v_mfma_i32_16x16x64_i8 v[94:97], v[106:109], v[192:195], v[94:97]
	v_mfma_i32_16x16x64_i8 v[90:93], v[114:117], v[192:195], v[90:93]
	s_waitcnt lgkmcnt(1)
	v_mfma_i32_16x16x64_i8 v[78:81], v[106:109], v[212:215], v[78:81]
	v_mfma_i32_16x16x64_i8 v[74:77], v[114:117], v[212:215], v[74:77]
	v_mfma_i32_16x16x64_i8 v[158:161], v[110:113], v[168:171], v[158:161]
	v_mfma_i32_16x16x64_i8 v[154:157], v[118:121], v[168:171], v[154:157]
	v_mfma_i32_16x16x64_i8 v[134:137], v[110:113], v[188:191], v[134:137]
	v_mfma_i32_16x16x64_i8 v[122:125], v[118:121], v[188:191], v[122:125]
	v_mfma_i32_16x16x64_i8 v[94:97], v[110:113], v[208:211], v[94:97]
	v_mfma_i32_16x16x64_i8 v[90:93], v[118:121], v[208:211], v[90:93]
	s_waitcnt lgkmcnt(0)
	v_mfma_i32_16x16x64_i8 v[78:81], v[110:113], v[216:219], v[78:81]
	v_mfma_i32_16x16x64_i8 v[74:77], v[118:121], v[216:219], v[74:77]
	s_setprio 0
	s_setprio 1
	v_mfma_i32_16x16x64_i8 v[150:153], v[126:129], v[164:167], v[150:153]
	v_mfma_i32_16x16x64_i8 v[146:149], v[138:141], v[164:167], v[146:149]
	v_mfma_i32_16x16x64_i8 v[102:105], v[126:129], v[184:187], v[102:105]
	v_mfma_i32_16x16x64_i8 v[98:101], v[138:141], v[184:187], v[98:101]
	v_mfma_i32_16x16x64_i8 v[86:89], v[126:129], v[192:195], v[86:89]
	v_mfma_i32_16x16x64_i8 v[82:85], v[138:141], v[192:195], v[82:85]
	v_mfma_i32_16x16x64_i8 v[70:73], v[126:129], v[212:215], v[70:73]
	v_mfma_i32_16x16x64_i8 v[66:69], v[138:141], v[212:215], v[66:69]
	v_mfma_i32_16x16x64_i8 v[150:153], v[130:133], v[168:171], v[150:153]
	v_mfma_i32_16x16x64_i8 v[146:149], v[142:145], v[168:171], v[146:149]
	v_mfma_i32_16x16x64_i8 v[102:105], v[130:133], v[188:191], v[102:105]
	v_mfma_i32_16x16x64_i8 v[98:101], v[142:145], v[188:191], v[98:101]
	v_mfma_i32_16x16x64_i8 v[86:89], v[130:133], v[208:211], v[86:89]
	v_mfma_i32_16x16x64_i8 v[82:85], v[142:145], v[208:211], v[82:85]
	v_mfma_i32_16x16x64_i8 v[70:73], v[130:133], v[216:219], v[70:73]
	v_mfma_i32_16x16x64_i8 v[66:69], v[142:145], v[216:219], v[66:69]
	s_setprio 0
	s_barrier
	s_mov_b32 s58, s85
	ds_read_b128 v[164:167], v178 offset:49152
	ds_read_b128 v[168:171], v178 offset:50176
	ds_read_b128 v[184:187], v178 offset:51200
	ds_read_b128 v[188:191], v178 offset:52224
	ds_read_b128 v[192:195], v178 offset:53248
	ds_read_b128 v[208:211], v178 offset:54272
	ds_read_b128 v[212:215], v178 offset:55296
	ds_read_b128 v[216:219], v178 offset:56320
	s_lshl1_add_u32 m0, s85, 0x18000
	s_mov_b32 s58, s85
	buffer_load_dwordx4 v173, s[64:67], s54 offen lds
	s_add_i32 s53, s53, 0xc000
	buffer_load_dwordx4 v173, s[64:67], s54 offen offset:1024 lds
	s_mov_b32 s54, s85
	s_lshl1_add_u32 m0, s85, 0x1c000
	s_mov_b32 s54, s85
	buffer_load_dwordx4 v173, s[64:67], s53 offen lds
	s_nop 0
	buffer_load_dwordx4 v173, s[64:67], s53 offen offset:1024 lds
	s_mov_b32 s53, s85
	s_add_i32 m0, s53, 0x8000
	s_mov_b32 s53, s85
	buffer_load_dwordx4 v172, s[88:91], s52 offen lds
	s_add_i32 m0, s53, 0xa000
	s_nop 0
	buffer_load_dwordx4 v174, s[88:91], s52 offen lds
	s_cmp_lg_u32 s55, 0
	s_cbranch_scc1 .Lgr19
	s_waitcnt vmcnt(8)
